# final norm row loop: the four weight vectors are loaded once before the loop (loop-invariant) so the three load/wait round trips after each row reduction are gone; plus previous changes
# speedup vs baseline: 1.0095x; 1.0021x over previous
; __device__ __forceinline__ float bf_lo(unsigned w) { return __uint_as_float(w << 16); }
; __device__ __forceinline__ float bf_hi(unsigned w) { return __uint_as_float(w & 0xffff0000u); }
;     __device__ __forceinline__ float* mods() const { return (float*)(ws + WS_MODS); }
;     __device__ __forceinline__ bf16_t* Y() const { return (bf16_t*)(ws + WS_Y); }
; __device__ __forceinline__ void phase_final(const Frame& F, const Params& P) {
;     for (int row = F.wg * 8 + F.wid; row < TL; row += F.nwg * 8) {
;         float* xr = P.out + (size_t)row * DM;
;         const float* g5 = F.mods() + (size_t)((NLAYER - 1) * 9 + (row >> 13)) * 6144 + 5 * 1024;
;         const bf16_t* yr = F.Y() + (size_t)row * 4 * DM;
;         f32x4 v[4]; float ss = 0.f;
; #pragma unroll
;         for (int j = 0; j < 4; ++j) {
;             const int col = F.lane * 4 + 256 * j;
;             v[j] = *(const f32x4*)(xr + col);
;             f32x4 s = (f32x4){0.f, 0.f, 0.f, 0.f};
; #pragma unroll
;             for (int k = 0; k < 4; ++k) { const u32x2 w = __builtin_nontemporal_load((const u32x2*)(yr + (size_t)k * DM + col));     s[0] += bf_lo(w.x); s[1] += bf_hi(w.x); s[2] += bf_lo(w.y); s[3] += bf_hi(w.y); }
;             v[j] += *(const f32x4*)(g5 + col) * s;
;             ss += v[j][0] * v[j][0] + v[j][1] * v[j][1] + v[j][2] * v[j][2] + v[j][3] * v[j][3];
.LBB0_1929:
	v_readlane_b32 s2, v252, 4
	v_readlane_b32 s3, v252, 5
	s_cmp_lt_i32 s2, 24
	s_cselect_b64 s[0:1], -1, 0
	s_cmp_gt_i32 s3, 23
	s_cselect_b64 s[2:3], -1, 0
	s_and_b64 s[0:1], s[0:1], s[2:3]
	s_and_b64 vcc, exec, s[0:1]
	s_cbranch_vccz .LBB0_1933
	v_readlane_b32 s1, v252, 8
	v_readfirstlane_b32 s0, v0
	s_ashr_i32 s0, s0, 6
	s_add_i32 s0, s0, s1
	s_cmp_gt_i32 s0, 0xffff
	s_cbranch_scc1 .LBB0_1933
	s_load_dwordx2 s[2:3], s[92:93], 0xd0
	v_lshlrev_b32_e32 v1, 2, v0
	s_waitcnt vmcnt(0)
	v_and_b32_e32 v6, 0xfc, v1
	v_mov_b32_e32 v5, 0
	v_lshlrev_b32_e32 v4, 2, v6
	s_ashr_i32 s1, s0, 31
	s_waitcnt lgkmcnt(0)
	v_lshl_add_u64 v[2:3], s[2:3], 0, v[4:5]
	s_lshl_b64 s[2:3], s[0:1], 13
	v_and_b32_e32 v7, 63, v0
	s_add_u32 s2, s54, s2
	v_lshlrev_b32_e32 v4, 3, v7
	s_addc_u32 s3, s55, s3
	v_lshl_add_u64 v[0:1], s[2:3], 0, v[4:5]
	s_mov_b64 s[2:3], 0x1c316100
	v_lshl_add_u64 v[0:1], v[0:1], 0, s[2:3]
	s_lshl_b64 s[2:3], s[0:1], 12
	s_add_u32 s2, s36, s2
	v_lshlrev_b32_e32 v4, 4, v7
	s_addc_u32 s3, s37, s3
	v_or_b32_e32 v8, 0x100, v6
	v_or_b32_e32 v12, 0x200, v6
	v_or_b32_e32 v14, 0x300, v6
	v_lshl_add_u64 v[4:5], s[2:3], 0, v[4:5]
	s_mov_b64 s[2:3], 0xc00
	v_readlane_b32 s8, v254, 40
	v_readlane_b32 s10, v254, 46
	v_lshl_add_u64 v[4:5], v[4:5], 0, s[2:3]
	s_movk_i32 s1, 0x1000
	v_lshlrev_b32_e32 v10, 2, v6
	v_lshlrev_b32_e32 v11, 2, v8
	v_lshlrev_b32_e32 v12, 2, v12
	v_lshlrev_b32_e32 v13, 2, v14
	v_mov_b32_e32 v14, 0x358637bd
	s_mov_b32 s2, 0x800000
	v_readlane_b32 s6, v254, 44
	v_readlane_b32 s9, v254, 41
	v_readlane_b32 s11, v254, 47
	v_readlane_b32 s7, v254, 45
	global_load_dwordx4 v[98:101], v[2:3], off
	global_load_dwordx4 v[102:105], v[2:3], off offset:1024
	global_load_dwordx4 v[106:109], v[2:3], off offset:2048
	global_load_dwordx4 v[110:113], v[2:3], off offset:3072
.LBB0_1932:
	s_ashr_i32 s3, s0, 13
	v_add_co_u32_e32 v36, vcc, s1, v0
	s_add_i32 s3, s3, 9
	global_load_dwordx2 v[8:9], v[0:1], off nt
	global_load_dwordx2 v[6:7], v[0:1], off offset:2048 nt
	global_load_dwordx2 v[52:53], v[0:1], off offset:512 nt
	global_load_dwordx2 v[54:55], v[0:1], off offset:2560 nt
	global_load_dwordx2 v[56:57], v[0:1], off offset:1024 nt
	global_load_dwordx2 v[58:59], v[0:1], off offset:3072 nt
	global_load_dwordx2 v[60:61], v[0:1], off offset:1536 nt
	global_load_dwordx2 v[62:63], v[0:1], off offset:3584 nt
	v_addc_co_u32_e32 v37, vcc, 0, v1, vcc
	s_mul_hi_i32 s4, s3, 0x6000
	s_mulk_i32 s3, 0x6000
	global_load_dwordx4 v[16:19], v[4:5], off offset:-3072
	global_load_dwordx4 v[20:23], v[4:5], off offset:-2048
	global_load_dwordx4 v[24:27], v[4:5], off offset:-1024
	global_load_dwordx4 v[28:31], v[4:5], off
	global_load_dwordx2 v[64:65], v[36:37], off nt
	global_load_dwordx2 v[66:67], v[36:37], off offset:2048 nt
	global_load_dwordx2 v[68:69], v[36:37], off offset:512 nt
	global_load_dwordx2 v[70:71], v[36:37], off offset:2560 nt
	global_load_dwordx2 v[72:73], v[36:37], off offset:1024 nt
	global_load_dwordx2 v[74:75], v[36:37], off offset:3072 nt
	global_load_dwordx2 v[76:77], v[36:37], off offset:1536 nt
	global_load_dwordx2 v[78:79], v[36:37], off offset:3584 nt
	s_add_u32 s3, s54, s3
	s_addc_u32 s5, s55, s4
	s_add_u32 s4, s3, 0x45000
	s_addc_u32 s5, s5, 0
	global_load_dwordx4 v[36:39], v10, s[4:5]
	global_load_dwordx4 v[40:43], v11, s[4:5]
	global_load_dwordx4 v[44:47], v12, s[4:5]
	global_load_dwordx4 v[48:51], v13, s[4:5]
	s_add_i32 s0, s0, s6
	v_lshl_add_u64 v[0:1], v[0:1], 0, s[8:9]
	s_cmp_lt_i32 s0, 0x10000
	s_waitcnt vmcnt(23)
	v_lshlrev_b32_e32 v80, 16, v8
	v_and_b32_e32 v81, 0xffff0000, v8
	v_lshlrev_b32_e32 v8, 16, v9
	v_and_b32_e32 v9, 0xffff0000, v9
	s_waitcnt vmcnt(21)
	v_lshlrev_b32_e32 v84, 16, v52
	v_and_b32_e32 v85, 0xffff0000, v52
	v_lshlrev_b32_e32 v82, 16, v6
	v_and_b32_e32 v83, 0xffff0000, v6
	v_lshlrev_b32_e32 v6, 16, v7
	v_and_b32_e32 v7, 0xffff0000, v7
	s_waitcnt vmcnt(20)
	v_lshlrev_b32_e32 v86, 16, v54
	v_and_b32_e32 v87, 0xffff0000, v54
	v_lshlrev_b32_e32 v52, 16, v53
	v_and_b32_e32 v53, 0xffff0000, v53
	s_waitcnt vmcnt(19)
	v_lshlrev_b32_e32 v88, 16, v56
	v_and_b32_e32 v89, 0xffff0000, v56
	v_lshlrev_b32_e32 v56, 16, v57
	v_and_b32_e32 v57, 0xffff0000, v57
	s_waitcnt vmcnt(17)
	v_lshlrev_b32_e32 v92, 16, v60
	v_and_b32_e32 v93, 0xffff0000, v60
	v_lshlrev_b32_e32 v60, 16, v61
	v_and_b32_e32 v61, 0xffff0000, v61
	v_pk_add_f32 v[80:81], v[80:81], 0 op_sel_hi:[1,0]
	v_pk_add_f32 v[8:9], v[8:9], 0 op_sel_hi:[1,0]
	v_pk_add_f32 v[84:85], v[84:85], 0 op_sel_hi:[1,0]
	v_lshlrev_b32_e32 v54, 16, v55
	v_and_b32_e32 v55, 0xffff0000, v55
	v_lshlrev_b32_e32 v90, 16, v58
	v_and_b32_e32 v91, 0xffff0000, v58
	v_lshlrev_b32_e32 v58, 16, v59
	v_and_b32_e32 v59, 0xffff0000, v59
	s_waitcnt vmcnt(16)
	v_lshlrev_b32_e32 v94, 16, v62
	v_and_b32_e32 v95, 0xffff0000, v62
	v_lshlrev_b32_e32 v62, 16, v63
	v_and_b32_e32 v63, 0xffff0000, v63
	v_pk_add_f32 v[52:53], v[52:53], 0 op_sel_hi:[1,0]
	v_pk_add_f32 v[88:89], v[88:89], 0 op_sel_hi:[1,0]
	v_pk_add_f32 v[56:57], v[56:57], 0 op_sel_hi:[1,0]
	v_pk_add_f32 v[92:93], v[92:93], 0 op_sel_hi:[1,0]
	v_pk_add_f32 v[60:61], v[60:61], 0 op_sel_hi:[1,0]
	v_pk_add_f32 v[80:81], v[80:81], v[82:83]
	s_waitcnt vmcnt(11)
; __device__ __forceinline__ float bf_lo(unsigned w) { return __uint_as_float(w << 16); }
; __device__ __forceinline__ float bf_hi(unsigned w) { return __uint_as_float(w & 0xffff0000u); }
; __device__ __forceinline__ void phase_final(const Frame& F, const Params& P) {
;     ...
;         for (int j = 0; j < 4; ++j) {
;             const int col = F.lane * 4 + 256 * j;
;             v[j] = *(const f32x4*)(xr + col);
;             f32x4 s = (f32x4){0.f, 0.f, 0.f, 0.f};
; #pragma unroll
;             for (int k = 0; k < 4; ++k) { const u32x2 w = __builtin_nontemporal_load((const u32x2*)(yr + (size_t)k * DM + col));     s[0] += bf_lo(w.x); s[1] += bf_hi(w.x); s[2] += bf_lo(w.y); s[3] += bf_hi(w.y); }
;             v[j] += *(const f32x4*)(g5 + col) * s;
;             ss += v[j][0] * v[j][0] + v[j][1] * v[j][1] + v[j][2] * v[j][2] + v[j][3] * v[j][3];
;         }
;         ss = wave_sum(ss);
;         const float rstd = rsqrtf(ss * (1.f / 1024.f) + EPS);
; #pragma unroll
;         for (int j = 0; j < 4; ++j) {
;             const int col = F.lane * 4 + 256 * j;
;             const f32x4 gg = *(const f32x4*)(P.g_final + col);
;             f32x4 o;
; #pragma unroll
;             for (int i = 0; i < 4; ++i) o[i] = v[j][i] * rstd * gg[i];
;             *(f32x4*)(xr + col) = o;
;         }
	v_lshlrev_b32_e32 v82, 16, v64
	v_and_b32_e32 v83, 0xffff0000, v64
	s_waitcnt vmcnt(10)
	v_lshlrev_b32_e32 v96, 16, v66
	v_and_b32_e32 v97, 0xffff0000, v66
	v_pk_add_f32 v[6:7], v[8:9], v[6:7]
	v_lshlrev_b32_e32 v8, 16, v65
	v_and_b32_e32 v9, 0xffff0000, v65
	v_lshlrev_b32_e32 v64, 16, v67
	v_and_b32_e32 v65, 0xffff0000, v67
	v_pk_add_f32 v[66:67], v[84:85], v[86:87]
	s_waitcnt vmcnt(9)
	v_lshlrev_b32_e32 v84, 16, v68
	v_and_b32_e32 v85, 0xffff0000, v68
	s_waitcnt vmcnt(8)
	v_lshlrev_b32_e32 v86, 16, v70
	v_and_b32_e32 v87, 0xffff0000, v70
	v_pk_add_f32 v[52:53], v[52:53], v[54:55]
	v_lshlrev_b32_e32 v54, 16, v69
	v_and_b32_e32 v55, 0xffff0000, v69
	v_lshlrev_b32_e32 v68, 16, v71
	v_and_b32_e32 v69, 0xffff0000, v71
	v_pk_add_f32 v[70:71], v[88:89], v[90:91]
	s_waitcnt vmcnt(7)
	v_lshlrev_b32_e32 v88, 16, v72
	v_and_b32_e32 v89, 0xffff0000, v72
	s_waitcnt vmcnt(6)
	v_lshlrev_b32_e32 v90, 16, v74
	v_and_b32_e32 v91, 0xffff0000, v74
	v_pk_add_f32 v[56:57], v[56:57], v[58:59]
	v_lshlrev_b32_e32 v58, 16, v73
	v_and_b32_e32 v59, 0xffff0000, v73
	v_lshlrev_b32_e32 v72, 16, v75
	v_and_b32_e32 v73, 0xffff0000, v75
	v_pk_add_f32 v[74:75], v[92:93], v[94:95]
	s_waitcnt vmcnt(5)
	v_lshlrev_b32_e32 v92, 16, v76
	v_and_b32_e32 v93, 0xffff0000, v76
	s_waitcnt vmcnt(4)
	v_lshlrev_b32_e32 v94, 16, v78
	v_and_b32_e32 v95, 0xffff0000, v78
	v_pk_add_f32 v[60:61], v[60:61], v[62:63]
	v_lshlrev_b32_e32 v62, 16, v77
	v_and_b32_e32 v63, 0xffff0000, v77
	v_lshlrev_b32_e32 v76, 16, v79
	v_and_b32_e32 v77, 0xffff0000, v79
	v_pk_add_f32 v[78:79], v[80:81], v[82:83]
	v_pk_add_f32 v[6:7], v[6:7], v[8:9]
	v_pk_add_f32 v[8:9], v[66:67], v[84:85]
	v_pk_add_f32 v[52:53], v[52:53], v[54:55]
	v_pk_add_f32 v[54:55], v[70:71], v[88:89]
	v_pk_add_f32 v[60:61], v[60:61], v[62:63]
	v_pk_add_f32 v[62:63], v[78:79], v[96:97]
	v_pk_add_f32 v[8:9], v[8:9], v[86:87]
	v_pk_add_f32 v[56:57], v[56:57], v[58:59]
	v_pk_add_f32 v[58:59], v[74:75], v[92:93]
	v_pk_add_f32 v[54:55], v[54:55], v[90:91]
	s_waitcnt vmcnt(3)
	v_pk_fma_f32 v[16:17], v[36:37], v[62:63], v[16:17]
	s_waitcnt vmcnt(2)
	v_pk_fma_f32 v[20:21], v[40:41], v[8:9], v[20:21]
	v_pk_add_f32 v[6:7], v[6:7], v[64:65]
	v_pk_add_f32 v[52:53], v[52:53], v[68:69]
	v_pk_add_f32 v[58:59], v[58:59], v[94:95]
	s_waitcnt vmcnt(1)
	v_pk_fma_f32 v[24:25], v[44:45], v[54:55], v[24:25]
	v_mul_f32_e32 v8, v17, v17
	v_mul_f32_e32 v9, v21, v21
	v_pk_add_f32 v[56:57], v[56:57], v[72:73]
	v_pk_add_f32 v[60:61], v[60:61], v[76:77]
	v_pk_fma_f32 v[6:7], v[38:39], v[6:7], v[18:19]
	v_pk_fma_f32 v[18:19], v[42:43], v[52:53], v[22:23]
	s_waitcnt vmcnt(0)
	v_pk_fma_f32 v[28:29], v[48:49], v[58:59], v[28:29]
	v_mul_f32_e32 v15, v25, v25
	v_fmac_f32_e32 v8, v16, v16
	v_fmac_f32_e32 v9, v20, v20
	v_pk_fma_f32 v[22:23], v[46:47], v[56:57], v[26:27]
	v_pk_fma_f32 v[26:27], v[50:51], v[60:61], v[30:31]
	v_mul_f32_e32 v30, v29, v29
	v_fmac_f32_e32 v15, v24, v24
	v_fmac_f32_e32 v8, v6, v6
	v_fmac_f32_e32 v9, v18, v18
	v_fmac_f32_e32 v30, v28, v28
	v_fmac_f32_e32 v15, v22, v22
	v_fmac_f32_e32 v8, v7, v7
	v_fmac_f32_e32 v9, v19, v19
	v_fmac_f32_e32 v30, v26, v26
	v_fmac_f32_e32 v15, v23, v23
	v_add_f32_e32 v8, v8, v9
	v_fmac_f32_e32 v30, v27, v27
	v_add_f32_e32 v8, v8, v15
	v_add_f32_e32 v8, v8, v30
	s_nop 1
	v_add_f32_dpp v8, v8, v8 quad_perm:[1,0,3,2] row_mask:0xf bank_mask:0xf bound_ctrl:1
	s_nop 1
	v_add_f32_dpp v8, v8, v8 quad_perm:[2,3,0,1] row_mask:0xf bank_mask:0xf bound_ctrl:1
	s_nop 1
	v_add_f32_dpp v8, v8, v8 row_half_mirror row_mask:0xf bank_mask:0xf bound_ctrl:1
	s_nop 1
	v_add_f32_dpp v8, v8, v8 row_mirror row_mask:0xf bank_mask:0xf bound_ctrl:1
	v_mov_b32_e32 v9, v8
	s_nop 1
	v_permlane16_swap_b32_e32 v8, v9
	v_add_f32_e32 v8, v8, v9
	v_mov_b32_e32 v9, v8
	s_nop 1
	v_permlane32_swap_b32_e32 v8, v9
	v_add_f32_e32 v8, v8, v9
	v_fmamk_f32 v8, v8, 0x3a800000, v14
	v_mul_f32_e32 v9, 0x4b800000, v8
	v_cmp_gt_f32_e32 vcc, s2, v8
	s_nop 1
	v_cndmask_b32_e32 v8, v8, v9, vcc
	v_rsq_f32_e32 v8, v8
	s_nop 0
	v_mul_f32_e32 v9, 0x45800000, v8
	v_cndmask_b32_e32 v30, v8, v9, vcc
	v_pk_mul_f32 v[16:17], v[16:17], v[30:31] op_sel_hi:[1,0]
	v_pk_mul_f32 v[6:7], v[6:7], v[30:31] op_sel_hi:[1,0]
	s_nop 0
	v_pk_mul_f32 v[8:9], v[100:101], v[6:7]
	v_pk_mul_f32 v[6:7], v[98:99], v[16:17]
	global_store_dwordx4 v[4:5], v[6:9], off offset:-3072
	v_pk_mul_f32 v[16:17], v[18:19], v[30:31] op_sel_hi:[1,0]
	v_pk_mul_f32 v[18:19], v[20:21], v[30:31] op_sel_hi:[1,0]
	s_nop 0
	v_pk_mul_f32 v[34:35], v[104:105], v[16:17]
	v_pk_mul_f32 v[32:33], v[102:103], v[18:19]
	global_store_dwordx4 v[4:5], v[32:35], off offset:-2048
	v_pk_mul_f32 v[16:17], v[22:23], v[30:31] op_sel_hi:[1,0]
	v_pk_mul_f32 v[18:19], v[24:25], v[30:31] op_sel_hi:[1,0]
	s_nop 0
	v_pk_mul_f32 v[46:47], v[108:109], v[16:17]
	v_pk_mul_f32 v[44:45], v[106:107], v[18:19]
	global_store_dwordx4 v[4:5], v[44:47], off offset:-1024
	v_pk_mul_f32 v[16:17], v[26:27], v[30:31] op_sel_hi:[1,0]
	v_pk_mul_f32 v[18:19], v[28:29], v[30:31] op_sel_hi:[1,0]
	s_nop 0
	v_pk_mul_f32 v[42:43], v[112:113], v[16:17]
	v_pk_mul_f32 v[40:41], v[110:111], v[18:19]
	global_store_dwordx4 v[4:5], v[40:43], off
	v_lshl_add_u64 v[4:5], v[4:5], 0, s[10:11]
	s_cbranch_scc1 .LBB0_1932
